# speedup vs baseline: 1.0615x; 1.0615x over previous
.LBB0_55:
	s_waitcnt lgkmcnt(14)
	v_mfma_f32_16x16x32_f16 v[102:105], v[30:33], v[82:85], 0
	s_mul_i32 s40, s3, 13
	s_add_i32 s6, s42, s40
	s_lshl_b32 s6, s6, 8
	s_waitcnt lgkmcnt(11)
	v_mfma_f32_16x16x32_f16 v[110:113], v[46:49], v[82:85], 0
	s_lshl_b32 s38, s33, 6
	s_or_b32 s6, s6, s38
	v_mul_u32_u24_e32 v186, 0x650, v206
	s_waitcnt lgkmcnt(7)
	v_mfma_f32_16x16x32_f16 v[162:165], v[54:57], v[82:85], 0
	v_cmp_eq_u32_e64 s[14:15], 0, v1
	s_waitcnt lgkmcnt(3)
	v_mfma_f32_16x16x32_f16 v[82:85], v[62:65], v[82:85], 0
	v_mfma_f32_16x16x32_f16 v[102:105], v[22:25], v[78:81], v[102:105]
	v_mfma_f32_16x16x32_f16 v[110:113], v[34:37], v[78:81], v[110:113]
	v_mfma_f32_16x16x32_f16 v[162:165], v[50:53], v[78:81], v[162:165]
	s_waitcnt lgkmcnt(2)
	v_mfma_f32_16x16x32_f16 v[78:81], v[58:61], v[78:81], v[82:85]
	v_mfma_f32_16x16x32_f16 v[82:85], v[18:21], v[74:77], v[102:105]
	v_mfma_f32_16x16x32_f16 v[102:105], v[26:29], v[74:77], v[110:113]
	v_mfma_f32_16x16x32_f16 v[110:113], v[38:41], v[74:77], v[162:165]
	s_waitcnt lgkmcnt(1)
	v_mfma_f32_16x16x32_f16 v[74:77], v[42:45], v[74:77], v[78:81]
	s_nop 0
	v_or_b32_e32 v162, s6, v1
	v_mfma_f32_16x16x32_f16 v[78:81], v[14:17], v[70:73], v[82:85]
	v_mfma_f32_16x16x32_f16 v[82:85], v[2:5], v[70:73], v[102:105]
	v_mfma_f32_16x16x32_f16 v[102:105], v[6:9], v[70:73], v[110:113]
	s_nop 5
	v_max_f32_e32 v89, v79, v79
	v_max_f32_e32 v163, v78, v78
	v_max_f32_e32 v89, v163, v89
	v_max3_f32 v89, v89, v80, v81
	v_max3_f32 v89, v89, v82, v83
	s_waitcnt lgkmcnt(0)
	v_mfma_f32_16x16x32_f16 v[70:73], v[10:13], v[70:73], v[74:77]
	v_max3_f32 v89, v89, v84, v85
	v_max3_f32 v89, v89, v102, v103
	v_max3_f32 v89, v89, v104, v105
	v_ashrrev_i32_e32 v163, 31, v162
	s_nop 3
	v_max3_f32 v74, v89, v70, v71
	v_max3_f32 v74, v74, v72, v73
	v_mov_b32_e32 v75, v74
	s_nop 1
	v_permlane16_swap_b32_e32 v74, v75
	v_max_f32_e32 v75, v75, v75
	v_max_f32_e32 v74, v74, v74
	v_max_f32_e32 v74, v74, v75
	v_mov_b32_e32 v75, v74
	s_nop 1
	v_permlane32_swap_b32_e32 v74, v75
	v_max_f32_e32 v75, v75, v75
	v_max_f32_e32 v74, v74, v74
	v_max_f32_e32 v74, v74, v75
	v_mul_f32_e32 v89, 0xbfb8aa3b, v74
	v_fmamk_f32 v74, v78, 0x3fb8aa3b, v89
	v_exp_f32_e32 v74, v74
	v_fmamk_f32 v75, v79, 0x3fb8aa3b, v89
	v_exp_f32_e32 v75, v75
	v_fmamk_f32 v76, v80, 0x3fb8aa3b, v89
	v_exp_f32_e32 v76, v76
	v_fmamk_f32 v77, v81, 0x3fb8aa3b, v89
	v_exp_f32_e32 v77, v77
	v_add_f32_e32 v78, 0, v74
	v_add_f32_e32 v78, v75, v78
	v_add_f32_e32 v78, v76, v78
	v_add_f32_e32 v110, v77, v78
	v_fmamk_f32 v78, v82, 0x3fb8aa3b, v89
	v_exp_f32_e32 v78, v78
	v_fmamk_f32 v79, v83, 0x3fb8aa3b, v89
	v_exp_f32_e32 v79, v79
	v_fmamk_f32 v80, v84, 0x3fb8aa3b, v89
	v_exp_f32_e32 v80, v80
	v_fmamk_f32 v81, v85, 0x3fb8aa3b, v89
	v_exp_f32_e32 v81, v81
	v_add_f32_e32 v82, v78, v110
	v_add_f32_e32 v82, v79, v82
	v_add_f32_e32 v82, v80, v82
	v_add_f32_e32 v110, v81, v82
	v_fmamk_f32 v82, v102, 0x3fb8aa3b, v89
	v_exp_f32_e32 v82, v82
	v_fmamk_f32 v83, v103, 0x3fb8aa3b, v89
	v_exp_f32_e32 v83, v83
	v_fmamk_f32 v84, v104, 0x3fb8aa3b, v89
	v_exp_f32_e32 v84, v84
	v_fmamk_f32 v85, v105, 0x3fb8aa3b, v89
	v_exp_f32_e32 v85, v85
	v_fmamk_f32 v70, v70, 0x3fb8aa3b, v89
	v_add_f32_e32 v102, v82, v110
	v_exp_f32_e32 v70, v70
	v_fmamk_f32 v71, v71, 0x3fb8aa3b, v89
	v_add_f32_e32 v102, v83, v102
	v_exp_f32_e32 v71, v71
	v_fmamk_f32 v72, v72, 0x3fb8aa3b, v89
	v_add_f32_e32 v102, v84, v102
	v_exp_f32_e32 v72, v72
	v_fmac_f32_e32 v89, 0x3fb8aa3b, v73
	v_add_f32_e32 v102, v85, v102
	v_exp_f32_e32 v73, v89
	v_add_f32_e32 v89, v70, v102
	v_add_f32_e32 v89, v71, v89
	v_add_f32_e32 v89, v72, v89
	v_add_f32_e32 v89, v73, v89
	v_mov_b32_e32 v102, v89
	s_nop 1
	v_permlane16_swap_b32_e32 v89, v102
	v_add_f32_e32 v89, v89, v102
	v_mov_b32_e32 v102, v89
	s_nop 1
	v_permlane32_swap_b32_e32 v89, v102
	v_add_f32_e32 v89, v89, v102
	v_rcp_f32_e32 v102, v89
	v_lshl_add_u64 v[104:105], v[162:163], 4, s[20:21]
	global_store_dwordx4 v[104:105], v[66:69], off sc0 sc1
	s_nop 1
	v_pk_mul_f32 v[66:67], v[102:103], v[74:75] op_sel_hi:[0,1]
	v_pk_mul_f32 v[68:69], v[102:103], v[76:77] op_sel_hi:[0,1]
	v_cvt_pk_f16_f32 v66, v66, v67
	v_cvt_pk_f16_f32 v67, v68, v69
	v_lshl_add_u32 v74, v87, 3, v186
	ds_write_b64 v74, v[66:67]
	v_pk_mul_f32 v[66:67], v[102:103], v[78:79] op_sel_hi:[0,1]
	v_pk_mul_f32 v[68:69], v[102:103], v[80:81] op_sel_hi:[0,1]
	v_cvt_pk_f16_f32 v66, v66, v67
	v_cvt_pk_f16_f32 v67, v68, v69
	ds_write_b64 v74, v[66:67] offset:6464
	v_pk_mul_f32 v[66:67], v[102:103], v[82:83] op_sel_hi:[0,1]
	v_pk_mul_f32 v[68:69], v[102:103], v[84:85] op_sel_hi:[0,1]
	v_cvt_pk_f16_f32 v66, v66, v67
	v_cvt_pk_f16_f32 v67, v68, v69
	ds_write_b64 v74, v[66:67] offset:12928
	v_pk_mul_f32 v[66:67], v[102:103], v[70:71] op_sel_hi:[0,1]
	v_pk_mul_f32 v[68:69], v[102:103], v[72:73] op_sel_hi:[0,1]
	v_cvt_pk_f16_f32 v66, v66, v67
	v_cvt_pk_f16_f32 v67, v68, v69
	ds_write_b64 v74, v[66:67] offset:19392
	s_waitcnt lgkmcnt(0)
	s_and_saveexec_b64 s[6:7], s[14:15]
	s_lshl_b32 s25, s42, 2
	s_add_i32 s25, s25, 0x14a00
	v_mov_b32_e32 v66, 1
	v_mov_b32_e32 v67, s25
	ds_write_b32 v67, v66
	s_or_b64 exec, exec, s[6:7]
	s_waitcnt vmcnt(11)
	v_ashrrev_i32_e32 v89, 31, v88
	v_or_b32_e32 v82, 0xc0, v87
	v_lshlrev_b64 v[66:67], 9, v[88:89]
	v_min_u32_e32 v82, 0xc7, v82
	v_lshl_add_u64 v[66:67], s[12:13], 0, v[66:67]
	v_lshlrev_b32_e32 v180, 2, v205
	v_mov_b32_e32 v181, 0
	v_add_u32_e32 v82, s37, v82
	v_lshl_add_u64 v[78:79], v[66:67], 0, v[180:181]
	v_ashrrev_i32_e32 v83, 31, v82
	global_load_dwordx4 v[174:177], v[78:79], off
	global_load_dwordx4 v[170:173], v[78:79], off offset:64
	global_load_dwordx4 v[166:169], v[78:79], off offset:128
	global_load_dwordx4 v[162:165], v[78:79], off offset:192
	global_load_dwordx4 v[66:69], v[78:79], off offset:256
	global_load_dwordx4 v[70:73], v[78:79], off offset:320
	global_load_dwordx4 v[74:77], v[78:79], off offset:384
	s_nop 0
	global_load_dwordx4 v[78:81], v[78:79], off offset:448
	v_lshl_add_u64 v[82:83], v[82:83], 2, s[8:9]
	s_waitcnt vmcnt(18)
	v_ashrrev_i32_e32 v87, 31, v86
	global_load_dword v182, v[82:83], off
	v_lshlrev_b64 v[82:83], 9, v[86:87]
	v_lshl_add_u64 v[82:83], s[12:13], 0, v[82:83]
	v_lshl_add_u64 v[184:185], v[82:83], 0, v[180:181]
	global_load_dwordx4 v[110:113], v[184:185], off
	global_load_dwordx4 v[102:105], v[184:185], off offset:64
	global_load_dwordx4 v[86:89], v[184:185], off offset:128
	global_load_dwordx4 v[82:85], v[184:185], off offset:192
	v_cvt_pk_f16_f32 v142, v142, v143
	v_cvt_pk_f16_f32 v143, v144, v145
	v_cvt_pk_f16_f32 v144, v138, v139
	v_cvt_pk_f16_f32 v145, v140, v141
	v_cvt_pk_f16_f32 v134, v134, v135
	v_cvt_pk_f16_f32 v135, v136, v137
	v_cvt_pk_f16_f32 v136, v130, v131
	v_cvt_pk_f16_f32 v137, v132, v133
	v_cvt_pk_f16_f32 v122, v122, v123
	v_cvt_pk_f16_f32 v123, v124, v125
	v_cvt_pk_f16_f32 v124, v118, v119
	v_cvt_pk_f16_f32 v125, v120, v121
	v_cvt_pk_f16_f32 v118, v90, v91
	v_cvt_pk_f16_f32 v119, v92, v93
	v_cvt_pk_f16_f32 v120, v94, v95
	v_cvt_pk_f16_f32 v121, v96, v97
	v_cndmask_b32_e64 v90, 0, 1, s[10:11]
	v_cmp_ne_u32_e64 s[6:7], 1, v90
	v_mov_b64_e32 v[90:91], v[142:143]
	s_andn2_b64 vcc, exec, s[10:11]
	v_mov_b64_e32 v[92:93], v[144:145]
	s_cbranch_vccnz .LBB0_59
	s_cmp_eq_u32 s33, 1
	s_cselect_b64 vcc, -1, 0
	s_cmp_eq_u32 s33, 2
	s_cselect_b64 s[8:9], -1, 0
	v_cndmask_b32_e64 v90, v118, v122, s[8:9]
	v_cndmask_b32_e64 v91, v119, v123, s[8:9]
	v_cndmask_b32_e64 v92, v120, v124, s[8:9]
	v_cndmask_b32_e64 v93, v121, v125, s[8:9]
	v_cndmask_b32_e32 v93, v93, v137, vcc
	v_cndmask_b32_e32 v92, v92, v136, vcc
	v_cndmask_b32_e32 v91, v91, v135, vcc
	v_cndmask_b32_e32 v90, v90, v134, vcc
.LBB0_59:
	v_mfma_f32_16x16x32_f16 v[94:97], v[30:33], v[142:145], 0
	s_add_i32 s8, s24, s40
	s_lshl_b32 s8, s8, 8
	s_or_b32 s8, s8, s38
	v_mfma_f32_16x16x32_f16 v[130:133], v[46:49], v[142:145], 0
	v_mfma_f32_16x16x32_f16 v[94:97], v[22:25], v[134:137], v[94:97]
	v_mfma_f32_16x16x32_f16 v[138:141], v[54:57], v[142:145], 0
	v_mfma_f32_16x16x32_f16 v[130:133], v[34:37], v[134:137], v[130:133]
	v_mfma_f32_16x16x32_f16 v[142:145], v[62:65], v[142:145], 0
	v_mfma_f32_16x16x32_f16 v[94:97], v[18:21], v[122:125], v[94:97]
	v_mfma_f32_16x16x32_f16 v[138:141], v[50:53], v[134:137], v[138:141]
	v_mfma_f32_16x16x32_f16 v[130:133], v[26:29], v[122:125], v[130:133]
	v_mfma_f32_16x16x32_f16 v[134:137], v[58:61], v[134:137], v[142:145]
	v_mfma_f32_16x16x32_f16 v[94:97], v[14:17], v[118:121], v[94:97]
	s_nop 2
	v_or_b32_e32 v142, s8, v1
	v_mfma_f32_16x16x32_f16 v[138:141], v[38:41], v[122:125], v[138:141]
	v_mfma_f32_16x16x32_f16 v[130:133], v[2:5], v[118:121], v[130:133]
	v_mfma_f32_16x16x32_f16 v[122:125], v[42:45], v[122:125], v[134:137]
	s_nop 2
	v_max_f32_e32 v134, v95, v95
	v_max_f32_e32 v135, v94, v94
	v_max_f32_e32 v134, v135, v134
	v_max3_f32 v134, v134, v96, v97
	v_max3_f32 v143, v134, v130, v131
	v_mfma_f32_16x16x32_f16 v[134:137], v[6:9], v[118:121], v[138:141]
	v_mfma_f32_16x16x32_f16 v[118:121], v[10:13], v[118:121], v[122:125]
	s_nop 1
	v_max3_f32 v138, v143, v132, v133
	s_nop 3
	v_max3_f32 v138, v138, v134, v135
	v_max3_f32 v138, v138, v136, v137
	v_ashrrev_i32_e32 v143, 31, v142
	v_max3_f32 v122, v138, v118, v119
	v_max3_f32 v122, v122, v120, v121
	v_mov_b32_e32 v123, v122
	s_nop 1
	v_permlane16_swap_b32_e32 v122, v123
	v_max_f32_e32 v123, v123, v123
	v_max_f32_e32 v122, v122, v122
	v_max_f32_e32 v122, v122, v123
	v_mov_b32_e32 v123, v122
	s_nop 1
	v_permlane32_swap_b32_e32 v122, v123
	v_max_f32_e32 v123, v123, v123
	v_max_f32_e32 v122, v122, v122
	v_max_f32_e32 v122, v122, v123
	v_mul_f32_e32 v138, 0xbfb8aa3b, v122
	v_fmamk_f32 v94, v94, 0x3fb8aa3b, v138
	v_exp_f32_e32 v94, v94
	v_fmamk_f32 v95, v95, 0x3fb8aa3b, v138
	v_exp_f32_e32 v95, v95
	v_fmamk_f32 v96, v96, 0x3fb8aa3b, v138
	v_exp_f32_e32 v96, v96
	v_fmamk_f32 v97, v97, 0x3fb8aa3b, v138
	v_exp_f32_e32 v97, v97
	v_add_f32_e32 v122, 0, v94
	v_add_f32_e32 v122, v95, v122
	v_add_f32_e32 v122, v96, v122
	v_add_f32_e32 v139, v97, v122
	v_fmamk_f32 v122, v130, 0x3fb8aa3b, v138
	v_exp_f32_e32 v122, v122
	v_fmamk_f32 v123, v131, 0x3fb8aa3b, v138
	v_exp_f32_e32 v123, v123
	v_fmamk_f32 v124, v132, 0x3fb8aa3b, v138
	v_exp_f32_e32 v124, v124
	v_fmamk_f32 v125, v133, 0x3fb8aa3b, v138
	v_exp_f32_e32 v125, v125
	v_add_f32_e32 v130, v122, v139
	v_add_f32_e32 v130, v123, v130
	v_add_f32_e32 v130, v124, v130
	v_add_f32_e32 v139, v125, v130
	v_fmamk_f32 v130, v134, 0x3fb8aa3b, v138
	v_exp_f32_e32 v130, v130
	v_fmamk_f32 v131, v135, 0x3fb8aa3b, v138
	v_exp_f32_e32 v131, v131
	v_fmamk_f32 v132, v136, 0x3fb8aa3b, v138
	v_exp_f32_e32 v132, v132
	v_fmamk_f32 v133, v137, 0x3fb8aa3b, v138
	v_exp_f32_e32 v133, v133
	v_fmamk_f32 v118, v118, 0x3fb8aa3b, v138
	v_add_f32_e32 v134, v130, v139
	v_exp_f32_e32 v118, v118
	v_fmamk_f32 v119, v119, 0x3fb8aa3b, v138
	v_add_f32_e32 v134, v131, v134
	v_exp_f32_e32 v119, v119
	v_fmamk_f32 v120, v120, 0x3fb8aa3b, v138
	v_add_f32_e32 v134, v132, v134
	v_exp_f32_e32 v120, v120
	v_fmac_f32_e32 v138, 0x3fb8aa3b, v121
	v_add_f32_e32 v134, v133, v134
	v_exp_f32_e32 v121, v138
	v_add_f32_e32 v134, v118, v134
	v_add_f32_e32 v134, v119, v134
	v_add_f32_e32 v134, v120, v134
	v_add_f32_e32 v134, v121, v134
	v_mov_b32_e32 v135, v134
	s_nop 1
	v_permlane16_swap_b32_e32 v134, v135
	v_add_f32_e32 v134, v134, v135
	v_mov_b32_e32 v135, v134
	s_nop 1
	v_permlane32_swap_b32_e32 v134, v135
	v_add_f32_e32 v134, v134, v135
	v_rcp_f32_e32 v134, v134
	v_lshl_add_u64 v[136:137], v[142:143], 4, s[20:21]
	global_store_dwordx4 v[136:137], v[90:93], off sc0 sc1
	s_nop 1
	v_pk_mul_f32 v[90:91], v[134:135], v[94:95] op_sel_hi:[0,1]
	v_pk_mul_f32 v[92:93], v[134:135], v[96:97] op_sel_hi:[0,1]
	v_cvt_pk_f16_f32 v90, v90, v91
	v_cvt_pk_f16_f32 v91, v92, v93
	v_lshl_add_u32 v94, v179, 3, v186
	ds_write_b64 v94, v[90:91]
	v_pk_mul_f32 v[90:91], v[134:135], v[122:123] op_sel_hi:[0,1]
	v_pk_mul_f32 v[92:93], v[134:135], v[124:125] op_sel_hi:[0,1]
	v_cvt_pk_f16_f32 v90, v90, v91
	v_cvt_pk_f16_f32 v91, v92, v93
	ds_write_b64 v94, v[90:91] offset:6464
	v_pk_mul_f32 v[90:91], v[134:135], v[130:131] op_sel_hi:[0,1]
	v_pk_mul_f32 v[92:93], v[134:135], v[132:133] op_sel_hi:[0,1]
	v_cvt_pk_f16_f32 v90, v90, v91
	v_cvt_pk_f16_f32 v91, v92, v93
	ds_write_b64 v94, v[90:91] offset:12928
	v_pk_mul_f32 v[90:91], v[134:135], v[118:119] op_sel_hi:[0,1]
	v_pk_mul_f32 v[92:93], v[134:135], v[120:121] op_sel_hi:[0,1]
	v_cvt_pk_f16_f32 v90, v90, v91
	v_cvt_pk_f16_f32 v91, v92, v93
	ds_write_b64 v94, v[90:91] offset:19392
	s_waitcnt lgkmcnt(0)
	s_and_saveexec_b64 s[8:9], s[14:15]
	s_lshl_b32 s10, s24, 2
	s_add_i32 s10, s10, 0x14a00
	v_mov_b32_e32 v90, 1
	v_mov_b32_e32 v91, s10
	ds_write_b32 v91, v90
	s_or_b64 exec, exec, s[8:9]
	s_waitcnt vmcnt(15)
	v_ashrrev_i32_e32 v179, 31, v178
	v_lshlrev_b64 v[90:91], 9, v[178:179]
	v_lshl_add_u64 v[90:91], s[12:13], 0, v[90:91]
	v_mov_b32_e32 v181, 0
	v_lshl_add_u64 v[178:179], v[90:91], 0, v[180:181]
	global_load_dwordx4 v[142:145], v[184:185], off offset:256
	global_load_dwordx4 v[138:141], v[184:185], off offset:320
	global_load_dwordx4 v[134:137], v[184:185], off offset:384
	global_load_dwordx4 v[130:133], v[184:185], off offset:448
	global_load_dwordx4 v[122:125], v[178:179], off
	global_load_dwordx4 v[118:121], v[178:179], off offset:64
	global_load_dwordx4 v[94:97], v[178:179], off offset:128
	global_load_dwordx4 v[90:93], v[178:179], off offset:192
	v_cvt_pk_f16_f32 v158, v158, v159
	v_cvt_pk_f16_f32 v159, v160, v161
	v_cvt_pk_f16_f32 v160, v154, v155
	v_cvt_pk_f16_f32 v161, v156, v157
	v_cvt_pk_f16_f32 v150, v150, v151
	v_cvt_pk_f16_f32 v151, v152, v153
	v_cvt_pk_f16_f32 v152, v146, v147
	v_cvt_pk_f16_f32 v153, v148, v149
	v_cvt_pk_f16_f32 v126, v126, v127
	v_cvt_pk_f16_f32 v127, v128, v129
	v_cvt_pk_f16_f32 v128, v114, v115
	v_cvt_pk_f16_f32 v129, v116, v117
	v_cvt_pk_f16_f32 v106, v106, v107
	v_cvt_pk_f16_f32 v107, v108, v109
	v_cvt_pk_f16_f32 v108, v98, v99
	v_cvt_pk_f16_f32 v109, v100, v101
	v_mov_b64_e32 v[98:99], v[158:159]
	s_and_b64 vcc, exec, s[6:7]
	v_mov_b64_e32 v[100:101], v[160:161]
	s_cbranch_vccnz .LBB0_63
	s_cmp_eq_u32 s33, 1
	s_cselect_b64 vcc, -1, 0
	s_cmp_eq_u32 s33, 2
	s_cselect_b64 s[8:9], -1, 0
	v_cndmask_b32_e64 v98, v106, v126, s[8:9]
	v_cndmask_b32_e64 v99, v107, v127, s[8:9]
	v_cndmask_b32_e64 v100, v108, v128, s[8:9]
	v_cndmask_b32_e64 v101, v109, v129, s[8:9]
	v_cndmask_b32_e32 v101, v101, v153, vcc
	v_cndmask_b32_e32 v100, v100, v152, vcc
	v_cndmask_b32_e32 v99, v99, v151, vcc
	v_cndmask_b32_e32 v98, v98, v150, vcc
.LBB0_63:
	v_mfma_f32_16x16x32_f16 v[114:117], v[30:33], v[158:161], 0
	s_add_i32 s8, s36, s40
	s_lshl_b32 s8, s8, 8
	s_or_b32 s8, s8, s38
	v_mfma_f32_16x16x32_f16 v[146:149], v[46:49], v[158:161], 0
	v_mfma_f32_16x16x32_f16 v[114:117], v[22:25], v[150:153], v[114:117]
	v_mfma_f32_16x16x32_f16 v[154:157], v[54:57], v[158:161], 0
	v_mfma_f32_16x16x32_f16 v[146:149], v[34:37], v[150:153], v[146:149]
	v_mfma_f32_16x16x32_f16 v[158:161], v[62:65], v[158:161], 0
	v_mfma_f32_16x16x32_f16 v[114:117], v[18:21], v[126:129], v[114:117]
	v_mfma_f32_16x16x32_f16 v[154:157], v[50:53], v[150:153], v[154:157]
	v_mfma_f32_16x16x32_f16 v[146:149], v[26:29], v[126:129], v[146:149]
	v_mfma_f32_16x16x32_f16 v[150:153], v[58:61], v[150:153], v[158:161]
	v_mfma_f32_16x16x32_f16 v[114:117], v[14:17], v[106:109], v[114:117]
	s_nop 2
	v_or_b32_e32 v158, s8, v1
	v_mfma_f32_16x16x32_f16 v[154:157], v[38:41], v[126:129], v[154:157]
	v_mfma_f32_16x16x32_f16 v[146:149], v[2:5], v[106:109], v[146:149]
	v_mfma_f32_16x16x32_f16 v[126:129], v[42:45], v[126:129], v[150:153]
	s_nop 2
	v_max_f32_e32 v150, v115, v115
	v_max_f32_e32 v151, v114, v114
	v_max_f32_e32 v150, v151, v150
	v_max3_f32 v150, v150, v116, v117
	v_max3_f32 v159, v150, v146, v147
	v_mfma_f32_16x16x32_f16 v[150:153], v[6:9], v[106:109], v[154:157]
	v_mfma_f32_16x16x32_f16 v[106:109], v[10:13], v[106:109], v[126:129]
	s_nop 1
	v_max3_f32 v154, v159, v148, v149
	s_nop 3
	v_max3_f32 v154, v154, v150, v151
	v_max3_f32 v154, v154, v152, v153
	v_ashrrev_i32_e32 v159, 31, v158
	v_max3_f32 v126, v154, v106, v107
	v_max3_f32 v126, v126, v108, v109
	v_mov_b32_e32 v127, v126
	s_nop 1
	v_permlane16_swap_b32_e32 v126, v127
	v_max_f32_e32 v127, v127, v127
	v_max_f32_e32 v126, v126, v126
	v_max_f32_e32 v126, v126, v127
	v_mov_b32_e32 v127, v126
	s_nop 1
	v_permlane32_swap_b32_e32 v126, v127
	v_max_f32_e32 v127, v127, v127
	v_max_f32_e32 v126, v126, v126
	v_max_f32_e32 v126, v126, v127
	v_mul_f32_e32 v154, 0xbfb8aa3b, v126
	v_fmamk_f32 v114, v114, 0x3fb8aa3b, v154
	v_exp_f32_e32 v114, v114
	v_fmamk_f32 v115, v115, 0x3fb8aa3b, v154
	v_exp_f32_e32 v115, v115
	v_fmamk_f32 v116, v116, 0x3fb8aa3b, v154
	v_exp_f32_e32 v116, v116
	v_fmamk_f32 v117, v117, 0x3fb8aa3b, v154
	v_exp_f32_e32 v117, v117
	v_add_f32_e32 v126, 0, v114
	v_add_f32_e32 v126, v115, v126
	v_add_f32_e32 v126, v116, v126
	v_add_f32_e32 v155, v117, v126
	v_fmamk_f32 v126, v146, 0x3fb8aa3b, v154
	v_exp_f32_e32 v126, v126
	v_fmamk_f32 v127, v147, 0x3fb8aa3b, v154
	v_exp_f32_e32 v127, v127
	v_fmamk_f32 v128, v148, 0x3fb8aa3b, v154
	v_exp_f32_e32 v128, v128
	v_fmamk_f32 v129, v149, 0x3fb8aa3b, v154
	v_exp_f32_e32 v129, v129
	v_add_f32_e32 v146, v126, v155
	v_add_f32_e32 v146, v127, v146
	v_add_f32_e32 v146, v128, v146
	v_add_f32_e32 v155, v129, v146
	v_fmamk_f32 v146, v150, 0x3fb8aa3b, v154
	v_exp_f32_e32 v146, v146
	v_fmamk_f32 v147, v151, 0x3fb8aa3b, v154
	v_exp_f32_e32 v147, v147
	v_fmamk_f32 v148, v152, 0x3fb8aa3b, v154
	v_exp_f32_e32 v148, v148
	v_fmamk_f32 v149, v153, 0x3fb8aa3b, v154
	v_exp_f32_e32 v149, v149
	v_fmamk_f32 v106, v106, 0x3fb8aa3b, v154
	v_add_f32_e32 v150, v146, v155
	v_exp_f32_e32 v106, v106
	v_fmamk_f32 v107, v107, 0x3fb8aa3b, v154
	v_add_f32_e32 v150, v147, v150
	v_exp_f32_e32 v107, v107
	v_fmamk_f32 v108, v108, 0x3fb8aa3b, v154
	v_add_f32_e32 v150, v148, v150
	v_exp_f32_e32 v108, v108
	v_fmac_f32_e32 v154, 0x3fb8aa3b, v109
	v_add_f32_e32 v150, v149, v150
	v_exp_f32_e32 v109, v154
	v_add_f32_e32 v150, v106, v150
	v_add_f32_e32 v150, v107, v150
	v_add_f32_e32 v150, v108, v150
	v_add_f32_e32 v150, v109, v150
	v_mov_b32_e32 v151, v150
	s_nop 1
	v_permlane16_swap_b32_e32 v150, v151
	v_add_f32_e32 v150, v150, v151
	v_mov_b32_e32 v151, v150
	s_nop 1
	v_permlane32_swap_b32_e32 v150, v151
	v_add_f32_e32 v150, v150, v151
	v_rcp_f32_e32 v150, v150
	v_lshl_add_u64 v[152:153], v[158:159], 4, s[20:21]
	global_store_dwordx4 v[152:153], v[98:101], off sc0 sc1
	s_nop 1
	v_pk_mul_f32 v[98:99], v[150:151], v[114:115] op_sel_hi:[0,1]
	v_pk_mul_f32 v[100:101], v[150:151], v[116:117] op_sel_hi:[0,1]
	v_cvt_pk_f16_f32 v98, v98, v99
	v_cvt_pk_f16_f32 v99, v100, v101
	v_lshl_add_u32 v114, v204, 3, v186
	ds_write_b64 v114, v[98:99]
	v_pk_mul_f32 v[98:99], v[150:151], v[126:127] op_sel_hi:[0,1]
	v_pk_mul_f32 v[100:101], v[150:151], v[128:129] op_sel_hi:[0,1]
	v_cvt_pk_f16_f32 v98, v98, v99
	v_cvt_pk_f16_f32 v99, v100, v101
	ds_write_b64 v114, v[98:99] offset:6464
	v_pk_mul_f32 v[98:99], v[150:151], v[146:147] op_sel_hi:[0,1]
	v_pk_mul_f32 v[100:101], v[150:151], v[148:149] op_sel_hi:[0,1]
	v_cvt_pk_f16_f32 v98, v98, v99
	v_cvt_pk_f16_f32 v99, v100, v101
	ds_write_b64 v114, v[98:99] offset:12928
	v_pk_mul_f32 v[98:99], v[150:151], v[106:107] op_sel_hi:[0,1]
	v_pk_mul_f32 v[100:101], v[150:151], v[108:109] op_sel_hi:[0,1]
	v_cvt_pk_f16_f32 v98, v98, v99
	v_cvt_pk_f16_f32 v99, v100, v101
	ds_write_b64 v114, v[98:99] offset:19392
	s_waitcnt lgkmcnt(0)
	s_and_saveexec_b64 s[8:9], s[14:15]
	s_lshl_b32 s10, s36, 2
	s_add_i32 s10, s10, 0x14a00
	v_mov_b32_e32 v98, 1
	v_mov_b32_e32 v99, s10
	ds_write_b32 v99, v98
	s_or_b64 exec, exec, s[8:9]
	global_load_dwordx4 v[158:161], v[178:179], off offset:256
	global_load_dwordx4 v[154:157], v[178:179], off offset:320
	global_load_dwordx4 v[150:153], v[178:179], off offset:384
	global_load_dwordx4 v[146:149], v[178:179], off offset:448
	v_mov_b32_e32 v181, 0
	s_waitcnt vmcnt(18)
	v_ashrrev_i32_e32 v183, 31, v182
	v_lshl_add_u64 v[98:99], s[12:13], 0, v[180:181]
	v_lshlrev_b64 v[100:101], 9, v[182:183]
	s_cmp_eq_u32 s42, 0
	v_lshl_add_u64 v[182:183], v[98:99], 0, v[100:101]
	s_cselect_b64 s[24:25], -1, 0
	s_cmp_lg_u32 s42, 0
	v_mov_b64_e32 v[98:99], v[174:175]
	v_mov_b64_e32 v[100:101], v[176:177]
	v_mov_b64_e32 v[106:107], v[170:171]
	v_mov_b64_e32 v[108:109], v[172:173]
	v_mov_b64_e32 v[114:115], v[166:167]
	v_mov_b64_e32 v[116:117], v[168:169]
	v_mov_b64_e32 v[126:127], v[162:163]
	v_mov_b64_e32 v[128:129], v[164:165]
	s_cbranch_scc1 .LBB0_67
	global_load_dwordx4 v[98:101], v[182:183], off
	global_load_dwordx4 v[106:109], v[182:183], off offset:64
	global_load_dwordx4 v[114:117], v[182:183], off offset:128
	global_load_dwordx4 v[126:129], v[182:183], off offset:192

.LBB0_69:
	v_mfma_f32_16x16x32_f16 v[188:191], v[30:33], v[174:177], 0
	s_add_i32 s12, s39, s40
	v_lshl_or_b32 v184, s12, 8, v1
	s_movk_i32 s12, 0xc8
	v_mfma_f32_16x16x32_f16 v[192:195], v[46:49], v[174:177], 0
	v_mfma_f32_16x16x32_f16 v[200:203], v[54:57], v[174:177], 0
	v_mfma_f32_16x16x32_f16 v[174:177], v[62:65], v[174:177], 0
	v_mfma_f32_16x16x32_f16 v[188:191], v[22:25], v[166:169], v[188:191]
	v_mfma_f32_16x16x32_f16 v[192:195], v[34:37], v[166:169], v[192:195]
	v_mfma_f32_16x16x32_f16 v[200:203], v[50:53], v[166:169], v[200:203]
	v_mfma_f32_16x16x32_f16 v[166:169], v[58:61], v[166:169], v[174:177]
	v_mfma_f32_16x16x32_f16 v[174:177], v[18:21], v[170:173], v[188:191]
	v_mfma_f32_16x16x32_f16 v[188:191], v[26:29], v[170:173], v[192:195]
	v_mfma_f32_16x16x32_f16 v[192:195], v[38:41], v[170:173], v[200:203]
	v_mfma_f32_16x16x32_f16 v[166:169], v[42:45], v[170:173], v[166:169]
	v_or_b32_e32 v170, s38, v184
	v_ashrrev_i32_e32 v171, 31, v170
	v_lshl_add_u64 v[184:185], v[170:171], 4, s[20:21]
	v_mfma_f32_16x16x32_f16 v[170:173], v[14:17], v[162:165], v[174:177]
	global_store_dwordx4 v[184:185], v[178:181], off sc0 sc1
	v_mfma_f32_16x16x32_f16 v[174:177], v[2:5], v[162:165], v[188:191]
	v_mfma_f32_16x16x32_f16 v[188:191], v[10:13], v[162:165], v[166:169]
	s_nop 4
	v_max_f32_e32 v178, v171, v171
	v_max_f32_e32 v179, v170, v170
	v_max_f32_e32 v178, v179, v178
	v_max3_f32 v178, v178, v172, v173
	v_max3_f32 v184, v178, v174, v175
	v_mfma_f32_16x16x32_f16 v[178:181], v[6:9], v[162:165], v[192:195]
	v_max3_f32 v184, v184, v176, v177
	s_nop 6
	v_max3_f32 v184, v184, v178, v179
	v_max3_f32 v184, v184, v180, v181
	v_max3_f32 v162, v184, v188, v189
	v_max3_f32 v162, v162, v190, v191
	v_mov_b32_e32 v163, v162
	s_nop 1
	v_permlane16_swap_b32_e32 v162, v163
	v_max_f32_e32 v163, v163, v163
	v_max_f32_e32 v162, v162, v162
	v_max_f32_e32 v162, v162, v163
	v_mov_b32_e32 v163, v162
	s_nop 1
	v_permlane32_swap_b32_e32 v162, v163
	v_max_f32_e32 v163, v163, v163
	v_max_f32_e32 v162, v162, v162
	v_max_f32_e32 v162, v162, v163
	v_mul_f32_e32 v184, 0xbfb8aa3b, v162
	v_fmamk_f32 v162, v170, 0x3fb8aa3b, v184
	v_exp_f32_e32 v162, v162
	v_fmamk_f32 v163, v171, 0x3fb8aa3b, v184
	v_exp_f32_e32 v163, v163
	v_fmamk_f32 v164, v172, 0x3fb8aa3b, v184
	v_exp_f32_e32 v164, v164
	v_fmamk_f32 v165, v173, 0x3fb8aa3b, v184
	v_exp_f32_e32 v165, v165
	v_add_f32_e32 v166, 0, v162
	v_add_f32_e32 v166, v163, v166
	v_add_f32_e32 v166, v164, v166
	v_add_f32_e32 v170, v165, v166
	v_fmamk_f32 v166, v174, 0x3fb8aa3b, v184
	v_exp_f32_e32 v166, v166
	v_fmamk_f32 v167, v175, 0x3fb8aa3b, v184
	v_exp_f32_e32 v167, v167
	v_fmamk_f32 v168, v176, 0x3fb8aa3b, v184
	v_exp_f32_e32 v168, v168
	v_fmamk_f32 v169, v177, 0x3fb8aa3b, v184
	v_exp_f32_e32 v169, v169
	v_add_f32_e32 v170, v166, v170
	v_add_f32_e32 v170, v167, v170
	v_add_f32_e32 v170, v168, v170
	v_add_f32_e32 v174, v169, v170
	v_fmamk_f32 v170, v178, 0x3fb8aa3b, v184
	v_exp_f32_e32 v170, v170
	v_fmamk_f32 v171, v179, 0x3fb8aa3b, v184
	v_exp_f32_e32 v171, v171
	v_fmamk_f32 v172, v180, 0x3fb8aa3b, v184
	v_exp_f32_e32 v172, v172
	v_fmamk_f32 v173, v181, 0x3fb8aa3b, v184
	v_exp_f32_e32 v173, v173
	v_add_f32_e32 v174, v170, v174
	v_add_f32_e32 v174, v171, v174
	v_add_f32_e32 v174, v172, v174
	v_add_f32_e32 v178, v173, v174
	v_fmamk_f32 v174, v188, 0x3fb8aa3b, v184
	v_exp_f32_e32 v174, v174
	v_fmamk_f32 v175, v189, 0x3fb8aa3b, v184
	v_exp_f32_e32 v175, v175
	v_fmamk_f32 v176, v190, 0x3fb8aa3b, v184
	v_exp_f32_e32 v176, v176
	v_fmac_f32_e32 v184, 0x3fb8aa3b, v191
	v_exp_f32_e32 v177, v184
	v_add_f32_e32 v178, v174, v178
	v_add_f32_e32 v178, v175, v178
	v_add_f32_e32 v178, v176, v178
	v_add_f32_e32 v179, v177, v178
	v_mov_b32_e32 v180, v179
	s_nop 1
	v_permlane16_swap_b32_e32 v179, v180
	v_add_f32_e32 v179, v179, v180
	v_or_b32_e32 v178, s41, v199
	v_mov_b32_e32 v180, v179
	s_nop 1
	v_permlane32_swap_b32_e32 v179, v180
	v_cmp_gt_u32_e32 vcc, s12, v178
	s_and_saveexec_b64 s[12:13], vcc
	s_cbranch_execz .LBB0_71
	v_add_f32_e32 v179, v179, v180
	v_rcp_f32_e32 v180, v179
	v_lshl_add_u32 v178, v178, 3, v186
	v_pk_mul_f32 v[162:163], v[180:181], v[162:163] op_sel_hi:[0,1]
	v_pk_mul_f32 v[164:165], v[180:181], v[164:165] op_sel_hi:[0,1]
	v_cvt_pk_f16_f32 v162, v162, v163
	v_cvt_pk_f16_f32 v163, v164, v165
	ds_write_b64 v178, v[162:163]
	v_pk_mul_f32 v[162:163], v[180:181], v[166:167] op_sel_hi:[0,1]
	v_pk_mul_f32 v[164:165], v[180:181], v[168:169] op_sel_hi:[0,1]
	v_cvt_pk_f16_f32 v162, v162, v163
	v_cvt_pk_f16_f32 v163, v164, v165
	ds_write_b64 v178, v[162:163] offset:6464
	v_pk_mul_f32 v[162:163], v[180:181], v[170:171] op_sel_hi:[0,1]
	v_pk_mul_f32 v[164:165], v[180:181], v[172:173] op_sel_hi:[0,1]
	v_cvt_pk_f16_f32 v162, v162, v163
	v_cvt_pk_f16_f32 v163, v164, v165
	ds_write_b64 v178, v[162:163] offset:12928
	v_pk_mul_f32 v[162:163], v[180:181], v[174:175] op_sel_hi:[0,1]
	v_pk_mul_f32 v[164:165], v[180:181], v[176:177] op_sel_hi:[0,1]
	v_cvt_pk_f16_f32 v162, v162, v163
	v_cvt_pk_f16_f32 v163, v164, v165
	ds_write_b64 v178, v[162:163] offset:19392

.LBB0_108:
	s_waitcnt vmcnt(18)
	v_cvt_pk_f16_f32 v110, v110, v111
	v_cvt_pk_f16_f32 v111, v112, v113
	s_waitcnt vmcnt(17)
	v_cvt_pk_f16_f32 v112, v102, v103
	v_cvt_pk_f16_f32 v113, v104, v105
	s_waitcnt vmcnt(16)
	v_cvt_pk_f16_f32 v86, v86, v87
	v_cvt_pk_f16_f32 v87, v88, v89
	v_mfma_f32_16x16x32_f16 v[102:105], v[30:33], v[110:113], 0
	s_waitcnt vmcnt(15)
	v_cvt_pk_f16_f32 v88, v82, v83
	v_cvt_pk_f16_f32 v89, v84, v85
	s_waitcnt vmcnt(13)
	v_cvt_pk_f16_f32 v82, v142, v143
	v_mfma_f32_16x16x32_f16 v[162:165], v[46:49], v[110:113], 0
	v_cvt_pk_f16_f32 v83, v144, v145
	s_waitcnt vmcnt(12)
	v_cvt_pk_f16_f32 v84, v138, v139
	v_cvt_pk_f16_f32 v85, v140, v141
	v_mfma_f32_16x16x32_f16 v[166:169], v[54:57], v[110:113], 0
	s_waitcnt vmcnt(11)
	v_cvt_pk_f16_f32 v134, v134, v135
	v_cvt_pk_f16_f32 v135, v136, v137
	s_waitcnt vmcnt(10)
	v_cvt_pk_f16_f32 v136, v130, v131
	v_mfma_f32_16x16x32_f16 v[102:105], v[22:25], v[86:89], v[102:105]
	v_cvt_pk_f16_f32 v137, v132, v133
	s_add_i32 s24, s36, 4
	s_add_i32 s25, s24, s40
	v_mfma_f32_16x16x32_f16 v[170:173], v[62:65], v[110:113], 0
	v_mfma_f32_16x16x32_f16 v[138:141], v[34:37], v[86:89], v[162:165]
	v_mfma_f32_16x16x32_f16 v[142:145], v[50:53], v[86:89], v[166:169]
	s_nop 1
	v_cndmask_b32_e64 v162, v137, v85, s[10:11]
	v_cndmask_b32_e64 v163, v136, v84, s[10:11]
	v_cndmask_b32_e64 v164, v135, v83, s[10:11]
	v_mfma_f32_16x16x32_f16 v[102:105], v[18:21], v[82:85], v[102:105]
	v_cndmask_b32_e64 v165, v134, v82, s[10:11]
	v_cndmask_b32_e64 v165, v165, v86, s[8:9]
	v_cndmask_b32_e64 v164, v164, v87, s[8:9]
	v_mfma_f32_16x16x32_f16 v[130:133], v[58:61], v[86:89], v[170:173]
	v_cndmask_b32_e64 v163, v163, v88, s[8:9]
	v_cndmask_b32_e64 v162, v162, v89, s[8:9]
	v_cndmask_b32_e64 v113, v162, v113, s[4:5]
	v_mfma_f32_16x16x32_f16 v[86:89], v[26:29], v[82:85], v[138:141]
	v_cndmask_b32_e64 v112, v163, v112, s[4:5]
	v_cndmask_b32_e64 v111, v164, v111, s[4:5]
	v_cndmask_b32_e64 v110, v165, v110, s[4:5]
	v_mfma_f32_16x16x32_f16 v[138:141], v[38:41], v[82:85], v[142:145]
	s_nop 2
	v_lshl_or_b32 v142, s25, 8, v1
	v_mfma_f32_16x16x32_f16 v[102:105], v[14:17], v[134:137], v[102:105]
	v_mfma_f32_16x16x32_f16 v[82:85], v[42:45], v[82:85], v[130:133]
	s_nop 2
	v_or_b32_e32 v130, s38, v142
	v_ashrrev_i32_e32 v131, 31, v130
	v_lshl_add_u64 v[130:131], v[130:131], 4, s[20:21]
	v_mfma_f32_16x16x32_f16 v[86:89], v[2:5], v[134:137], v[86:89]
	global_store_dwordx4 v[130:131], v[110:113], off sc0 sc1
	s_nop 1
	v_max_f32_e32 v110, v103, v103
	v_max_f32_e32 v111, v102, v102
	v_max_f32_e32 v110, v111, v110
	v_max3_f32 v110, v110, v104, v105
	s_nop 0
	v_max3_f32 v130, v110, v86, v87
	v_mfma_f32_16x16x32_f16 v[110:113], v[6:9], v[134:137], v[138:141]
	v_max3_f32 v130, v130, v88, v89
	s_nop 6
	v_max3_f32 v130, v130, v110, v111
	v_max3_f32 v138, v130, v112, v113
	v_mfma_f32_16x16x32_f16 v[130:133], v[10:13], v[134:137], v[82:85]
	s_nop 7
	v_max3_f32 v82, v138, v130, v131
	v_max3_f32 v82, v82, v132, v133
	v_mov_b32_e32 v83, v82
	s_nop 1
	v_permlane16_swap_b32_e32 v82, v83
	v_max_f32_e32 v83, v83, v83
	v_max_f32_e32 v82, v82, v82
	v_max_f32_e32 v82, v82, v83
	v_mov_b32_e32 v83, v82
	s_nop 1
	v_permlane32_swap_b32_e32 v82, v83
	v_max_f32_e32 v83, v83, v83
	v_max_f32_e32 v82, v82, v82
	v_max_f32_e32 v82, v82, v83
	v_mul_f32_e32 v134, 0xbfb8aa3b, v82
	v_fmamk_f32 v82, v102, 0x3fb8aa3b, v134
	v_exp_f32_e32 v82, v82
	v_fmamk_f32 v83, v103, 0x3fb8aa3b, v134
	v_exp_f32_e32 v83, v83
	v_fmamk_f32 v84, v104, 0x3fb8aa3b, v134
	v_exp_f32_e32 v84, v84
	v_fmamk_f32 v85, v105, 0x3fb8aa3b, v134
	v_exp_f32_e32 v85, v85
	v_fmamk_f32 v86, v86, 0x3fb8aa3b, v134
	v_add_f32_e32 v102, 0, v82
	v_exp_f32_e32 v86, v86
	v_fmamk_f32 v87, v87, 0x3fb8aa3b, v134
	v_add_f32_e32 v102, v83, v102
	v_exp_f32_e32 v87, v87
	v_fmamk_f32 v88, v88, 0x3fb8aa3b, v134
	v_add_f32_e32 v102, v84, v102
	v_exp_f32_e32 v88, v88
	v_fmamk_f32 v89, v89, 0x3fb8aa3b, v134
	v_add_f32_e32 v102, v85, v102
	v_exp_f32_e32 v89, v89
	v_add_f32_e32 v102, v86, v102
	v_add_f32_e32 v102, v87, v102
	v_add_f32_e32 v102, v88, v102
	v_add_f32_e32 v135, v89, v102
	v_fmamk_f32 v102, v110, 0x3fb8aa3b, v134
	v_exp_f32_e32 v102, v102
	v_fmamk_f32 v103, v111, 0x3fb8aa3b, v134
	v_exp_f32_e32 v103, v103
	v_fmamk_f32 v104, v112, 0x3fb8aa3b, v134
	v_exp_f32_e32 v104, v104
	v_fmamk_f32 v105, v113, 0x3fb8aa3b, v134
	v_exp_f32_e32 v105, v105
	v_add_f32_e32 v110, v102, v135
	v_add_f32_e32 v110, v103, v110
	v_add_f32_e32 v110, v104, v110
	v_add_f32_e32 v135, v105, v110
	v_fmamk_f32 v110, v130, 0x3fb8aa3b, v134
	v_exp_f32_e32 v110, v110
	v_fmamk_f32 v111, v131, 0x3fb8aa3b, v134
	v_exp_f32_e32 v111, v111
	v_fmamk_f32 v112, v132, 0x3fb8aa3b, v134
	v_exp_f32_e32 v112, v112
	v_fmac_f32_e32 v134, 0x3fb8aa3b, v133
	v_exp_f32_e32 v113, v134
	v_add_f32_e32 v130, v110, v135
	v_add_f32_e32 v130, v111, v130
	v_add_f32_e32 v130, v112, v130
	v_add_f32_e32 v131, v113, v130
	v_mov_b32_e32 v132, v131
	s_nop 1
	v_permlane16_swap_b32_e32 v131, v132
	v_add_f32_e32 v131, v131, v132
	v_lshl_or_b32 v130, s24, 4, v199
	v_mov_b32_e32 v132, v131
	s_movk_i32 s24, 0xc8
	s_nop 0
	v_permlane32_swap_b32_e32 v131, v132
	v_cmp_gt_u32_e32 vcc, s24, v130
	s_and_saveexec_b64 s[24:25], vcc
	s_cbranch_execz .LBB0_110
	v_add_f32_e32 v131, v131, v132
	v_rcp_f32_e32 v132, v131
	v_lshl_add_u32 v130, v130, 3, v186
	v_pk_mul_f32 v[82:83], v[132:133], v[82:83] op_sel_hi:[0,1]
	v_pk_mul_f32 v[84:85], v[132:133], v[84:85] op_sel_hi:[0,1]
	v_cvt_pk_f16_f32 v82, v82, v83
	v_cvt_pk_f16_f32 v83, v84, v85
	ds_write_b64 v130, v[82:83]
	v_pk_mul_f32 v[82:83], v[132:133], v[86:87] op_sel_hi:[0,1]
	v_pk_mul_f32 v[84:85], v[132:133], v[88:89] op_sel_hi:[0,1]
	v_cvt_pk_f16_f32 v82, v82, v83
	v_cvt_pk_f16_f32 v83, v84, v85
	ds_write_b64 v130, v[82:83] offset:6464
	v_pk_mul_f32 v[82:83], v[132:133], v[102:103] op_sel_hi:[0,1]
	v_pk_mul_f32 v[84:85], v[132:133], v[104:105] op_sel_hi:[0,1]
	v_cvt_pk_f16_f32 v82, v82, v83
	v_cvt_pk_f16_f32 v83, v84, v85
	ds_write_b64 v130, v[82:83] offset:12928
	v_pk_mul_f32 v[82:83], v[132:133], v[110:111] op_sel_hi:[0,1]
	v_pk_mul_f32 v[84:85], v[132:133], v[112:113] op_sel_hi:[0,1]
	v_cvt_pk_f16_f32 v82, v82, v83
	v_cvt_pk_f16_f32 v83, v84, v85
	ds_write_b64 v130, v[82:83] offset:19392

.LBB0_113:
	s_waitcnt vmcnt(9)
	v_cvt_pk_f16_f32 v82, v122, v123
	v_cvt_pk_f16_f32 v83, v124, v125
	s_waitcnt vmcnt(8)
	v_cvt_pk_f16_f32 v84, v118, v119
	v_cvt_pk_f16_f32 v85, v120, v121
	s_waitcnt vmcnt(7)
	v_cvt_pk_f16_f32 v94, v94, v95
	v_cvt_pk_f16_f32 v95, v96, v97
	v_mfma_f32_16x16x32_f16 v[86:89], v[30:33], v[82:85], 0
	s_waitcnt vmcnt(6)
	v_cvt_pk_f16_f32 v96, v90, v91
	v_cvt_pk_f16_f32 v97, v92, v93
	s_waitcnt vmcnt(4)
	v_cvt_pk_f16_f32 v90, v158, v159
	v_mfma_f32_16x16x32_f16 v[102:105], v[46:49], v[82:85], 0
	v_cvt_pk_f16_f32 v91, v160, v161
	s_waitcnt vmcnt(3)
	v_cvt_pk_f16_f32 v92, v154, v155
	v_cvt_pk_f16_f32 v93, v156, v157
	v_mfma_f32_16x16x32_f16 v[110:113], v[54:57], v[82:85], 0
	s_waitcnt vmcnt(2)
	v_cvt_pk_f16_f32 v122, v150, v151
	v_cvt_pk_f16_f32 v123, v152, v153
	s_waitcnt vmcnt(1)
	v_cvt_pk_f16_f32 v124, v146, v147
	v_mfma_f32_16x16x32_f16 v[86:89], v[22:25], v[94:97], v[86:89]
	v_cvt_pk_f16_f32 v125, v148, v149
	v_cndmask_b32_e64 v130, v125, v93, s[10:11]
	v_cndmask_b32_e64 v131, v124, v92, s[10:11]
	v_mfma_f32_16x16x32_f16 v[118:121], v[62:65], v[82:85], 0
	v_cndmask_b32_e64 v132, v123, v91, s[10:11]
	v_cndmask_b32_e64 v133, v122, v90, s[10:11]
	s_add_i32 s24, s36, 6
	v_mfma_f32_16x16x32_f16 v[102:105], v[34:37], v[94:97], v[102:105]
	v_cndmask_b32_e64 v133, v133, v94, s[8:9]
	v_cndmask_b32_e64 v132, v132, v95, s[8:9]
	v_cndmask_b32_e64 v131, v131, v96, s[8:9]
	v_mfma_f32_16x16x32_f16 v[110:113], v[50:53], v[94:97], v[110:113]
	v_cndmask_b32_e64 v130, v130, v97, s[8:9]
	v_cndmask_b32_e64 v85, v130, v85, s[4:5]
	v_cndmask_b32_e64 v84, v131, v84, s[4:5]
	v_mfma_f32_16x16x32_f16 v[86:89], v[18:21], v[90:93], v[86:89]
	v_cndmask_b32_e64 v83, v132, v83, s[4:5]
	v_cndmask_b32_e64 v82, v133, v82, s[4:5]
	s_add_i32 s4, s24, s40
	v_mfma_f32_16x16x32_f16 v[118:121], v[58:61], v[94:97], v[118:121]
	v_mfma_f32_16x16x32_f16 v[94:97], v[26:29], v[90:93], v[102:105]
	v_mfma_f32_16x16x32_f16 v[102:105], v[38:41], v[90:93], v[110:113]
	s_nop 2
	v_lshl_or_b32 v110, s4, 8, v1
	v_mfma_f32_16x16x32_f16 v[86:89], v[14:17], v[122:125], v[86:89]
	v_or_b32_e32 v110, s38, v110
	v_ashrrev_i32_e32 v111, 31, v110
	v_lshl_add_u64 v[110:111], v[110:111], 4, s[20:21]
	v_mfma_f32_16x16x32_f16 v[90:93], v[42:45], v[90:93], v[118:121]
	global_store_dwordx4 v[110:111], v[82:85], off sc0 sc1
	s_movk_i32 s4, 0xc8
	v_mfma_f32_16x16x32_f16 v[94:97], v[2:5], v[122:125], v[94:97]
	s_nop 0
	v_max_f32_e32 v82, v87, v87
	v_max_f32_e32 v83, v86, v86
	v_max_f32_e32 v82, v83, v82
	v_mfma_f32_16x16x32_f16 v[102:105], v[6:9], v[122:125], v[102:105]
	v_max3_f32 v82, v82, v88, v89
	s_nop 1
	v_max3_f32 v82, v82, v94, v95
	v_max3_f32 v82, v82, v96, v97
	v_mfma_f32_16x16x32_f16 v[110:113], v[10:13], v[122:125], v[90:93]
	s_nop 1
	v_max3_f32 v82, v82, v102, v103
	v_max3_f32 v82, v82, v104, v105
	s_nop 3
	v_max3_f32 v82, v82, v110, v111
	v_max3_f32 v82, v82, v112, v113
	v_mov_b32_e32 v83, v82
	s_nop 1
	v_permlane16_swap_b32_e32 v82, v83
	v_max_f32_e32 v83, v83, v83
	v_max_f32_e32 v82, v82, v82
	v_max_f32_e32 v82, v82, v83
	v_mov_b32_e32 v83, v82
	s_nop 1
	v_permlane32_swap_b32_e32 v82, v83
	v_max_f32_e32 v83, v83, v83
	v_max_f32_e32 v82, v82, v82
	v_max_f32_e32 v82, v82, v83
	v_mul_f32_e32 v118, 0xbfb8aa3b, v82
	v_fmamk_f32 v82, v86, 0x3fb8aa3b, v118
	v_exp_f32_e32 v82, v82
	v_fmamk_f32 v83, v87, 0x3fb8aa3b, v118
	v_exp_f32_e32 v83, v83
	v_fmamk_f32 v84, v88, 0x3fb8aa3b, v118
	v_exp_f32_e32 v84, v84
	v_fmamk_f32 v85, v89, 0x3fb8aa3b, v118
	v_exp_f32_e32 v85, v85
	v_add_f32_e32 v86, 0, v82
	v_add_f32_e32 v86, v83, v86
	v_add_f32_e32 v86, v84, v86
	v_add_f32_e32 v90, v85, v86
	v_fmamk_f32 v86, v94, 0x3fb8aa3b, v118
	v_exp_f32_e32 v86, v86
	v_fmamk_f32 v87, v95, 0x3fb8aa3b, v118
	v_exp_f32_e32 v87, v87
	v_fmamk_f32 v88, v96, 0x3fb8aa3b, v118
	v_exp_f32_e32 v88, v88
	v_fmamk_f32 v89, v97, 0x3fb8aa3b, v118
	v_exp_f32_e32 v89, v89
	v_add_f32_e32 v90, v86, v90
	v_add_f32_e32 v90, v87, v90
	v_add_f32_e32 v90, v88, v90
	v_add_f32_e32 v94, v89, v90
	v_fmamk_f32 v90, v102, 0x3fb8aa3b, v118
	v_exp_f32_e32 v90, v90
	v_fmamk_f32 v91, v103, 0x3fb8aa3b, v118
	v_exp_f32_e32 v91, v91
	v_fmamk_f32 v92, v104, 0x3fb8aa3b, v118
	v_exp_f32_e32 v92, v92
	v_fmamk_f32 v93, v105, 0x3fb8aa3b, v118
	v_exp_f32_e32 v93, v93
	v_add_f32_e32 v94, v90, v94
	v_add_f32_e32 v94, v91, v94
	v_add_f32_e32 v94, v92, v94
	v_add_f32_e32 v102, v93, v94
	v_fmamk_f32 v94, v110, 0x3fb8aa3b, v118
	v_exp_f32_e32 v94, v94
	v_fmamk_f32 v95, v111, 0x3fb8aa3b, v118
	v_exp_f32_e32 v95, v95
	v_fmamk_f32 v96, v112, 0x3fb8aa3b, v118
	v_exp_f32_e32 v96, v96
	v_fmac_f32_e32 v118, 0x3fb8aa3b, v113
	v_exp_f32_e32 v97, v118
	v_add_f32_e32 v102, v94, v102
	v_add_f32_e32 v102, v95, v102
	v_add_f32_e32 v102, v96, v102
	v_add_f32_e32 v103, v97, v102
	v_mov_b32_e32 v104, v103
	s_nop 1
	v_permlane16_swap_b32_e32 v103, v104
	v_add_f32_e32 v103, v103, v104
	v_lshl_or_b32 v102, s24, 4, v199
	v_mov_b32_e32 v104, v103
	s_nop 1
	v_permlane32_swap_b32_e32 v103, v104
	v_cmp_gt_u32_e32 vcc, s4, v102
	s_and_saveexec_b64 s[4:5], vcc
	s_cbranch_execz .LBB0_115
	v_add_f32_e32 v103, v103, v104
	v_rcp_f32_e32 v104, v103
	v_lshl_add_u32 v102, v102, 3, v186
	v_pk_mul_f32 v[82:83], v[104:105], v[82:83] op_sel_hi:[0,1]
	v_pk_mul_f32 v[84:85], v[104:105], v[84:85] op_sel_hi:[0,1]
	v_cvt_pk_f16_f32 v82, v82, v83
	v_cvt_pk_f16_f32 v83, v84, v85
	ds_write_b64 v102, v[82:83]
	v_pk_mul_f32 v[82:83], v[104:105], v[86:87] op_sel_hi:[0,1]
	v_pk_mul_f32 v[84:85], v[104:105], v[88:89] op_sel_hi:[0,1]
	v_cvt_pk_f16_f32 v82, v82, v83
	v_cvt_pk_f16_f32 v83, v84, v85
	ds_write_b64 v102, v[82:83] offset:6464
	v_pk_mul_f32 v[82:83], v[104:105], v[90:91] op_sel_hi:[0,1]
	v_pk_mul_f32 v[84:85], v[104:105], v[92:93] op_sel_hi:[0,1]
	v_cvt_pk_f16_f32 v82, v82, v83
	v_cvt_pk_f16_f32 v83, v84, v85
	ds_write_b64 v102, v[82:83] offset:12928
	v_pk_mul_f32 v[82:83], v[104:105], v[94:95] op_sel_hi:[0,1]
	v_pk_mul_f32 v[84:85], v[104:105], v[96:97] op_sel_hi:[0,1]
	v_cvt_pk_f16_f32 v82, v82, v83
	v_cvt_pk_f16_f32 v83, v84, v85
	ds_write_b64 v102, v[82:83] offset:19392

.LBB0_120:
	v_mfma_f32_16x16x32_f16 v[30:33], v[30:33], v[82:85], 0
	s_mul_i32 s4, s3, 0xd00
	s_addk_i32 s4, 0xc00
	v_mfma_f32_16x16x32_f16 v[46:49], v[46:49], v[82:85], 0
	v_mfma_f32_16x16x32_f16 v[54:57], v[54:57], v[82:85], 0
	v_mfma_f32_16x16x32_f16 v[22:25], v[22:25], v[86:89], v[30:33]
	v_mfma_f32_16x16x32_f16 v[62:65], v[62:65], v[82:85], 0
	v_mfma_f32_16x16x32_f16 v[30:33], v[34:37], v[86:89], v[46:49]
	v_mfma_f32_16x16x32_f16 v[34:37], v[50:53], v[86:89], v[54:57]
	v_mfma_f32_16x16x32_f16 v[18:21], v[18:21], v[90:93], v[22:25]
	v_mfma_f32_16x16x32_f16 v[46:49], v[58:61], v[86:89], v[62:65]
	v_mfma_f32_16x16x32_f16 v[22:25], v[26:29], v[90:93], v[30:33]
	v_mfma_f32_16x16x32_f16 v[26:29], v[38:41], v[90:93], v[34:37]
	s_nop 3
	v_or_b32_e32 v34, s4, v1
	v_mfma_f32_16x16x32_f16 v[14:17], v[14:17], v[66:69], v[18:21]
	v_or_b32_e32 v34, s38, v34
	v_ashrrev_i32_e32 v35, 31, v34
	v_lshl_add_u64 v[34:35], v[34:35], 4, s[20:21]
	v_mfma_f32_16x16x32_f16 v[30:33], v[42:45], v[90:93], v[46:49]
	global_store_dwordx4 v[34:35], v[70:73], off sc0 sc1
	s_nop 2
	v_max_f32_e32 v34, v15, v15
	v_max_f32_e32 v35, v14, v14
	v_mfma_f32_16x16x32_f16 v[18:21], v[2:5], v[66:69], v[22:25]
	v_max_f32_e32 v2, v35, v34
	v_max3_f32 v2, v2, v16, v17
	s_movk_i32 s4, 0xc8
	v_mfma_f32_16x16x32_f16 v[22:25], v[6:9], v[66:69], v[26:29]
	v_mfma_f32_16x16x32_f16 v[26:29], v[10:13], v[66:69], v[30:33]
	s_nop 2
	v_max3_f32 v2, v2, v18, v19
	v_max3_f32 v2, v2, v20, v21
	s_nop 1
	v_max3_f32 v2, v2, v22, v23
	v_max3_f32 v2, v2, v24, v25
	v_max3_f32 v2, v2, v26, v27
	v_max3_f32 v2, v2, v28, v29
	v_mov_b32_e32 v3, v2
	s_nop 1
	v_permlane16_swap_b32_e32 v2, v3
	v_max_f32_e32 v3, v3, v3
	v_max_f32_e32 v2, v2, v2
	v_max_f32_e32 v2, v2, v3
	v_mov_b32_e32 v3, v2
	s_nop 1
	v_permlane32_swap_b32_e32 v2, v3
	v_max_f32_e32 v3, v3, v3
	v_max_f32_e32 v2, v2, v2
	v_max_f32_e32 v2, v2, v3
	v_mul_f32_e32 v30, 0xbfb8aa3b, v2
	v_fmamk_f32 v2, v14, 0x3fb8aa3b, v30
	v_exp_f32_e32 v2, v2
	v_fmamk_f32 v3, v15, 0x3fb8aa3b, v30
	v_exp_f32_e32 v3, v3
	v_fmamk_f32 v4, v16, 0x3fb8aa3b, v30
	v_exp_f32_e32 v4, v4
	v_fmamk_f32 v5, v17, 0x3fb8aa3b, v30
	v_exp_f32_e32 v5, v5
	v_add_f32_e32 v6, 0, v2
	v_add_f32_e32 v6, v3, v6
	v_add_f32_e32 v6, v4, v6
	v_add_f32_e32 v10, v5, v6
	v_fmamk_f32 v6, v18, 0x3fb8aa3b, v30
	v_exp_f32_e32 v6, v6
	v_fmamk_f32 v7, v19, 0x3fb8aa3b, v30
	v_exp_f32_e32 v7, v7
	v_fmamk_f32 v8, v20, 0x3fb8aa3b, v30
	v_exp_f32_e32 v8, v8
	v_fmamk_f32 v9, v21, 0x3fb8aa3b, v30
	v_exp_f32_e32 v9, v9
	v_add_f32_e32 v10, v6, v10
	v_add_f32_e32 v10, v7, v10
	v_add_f32_e32 v10, v8, v10
	v_add_f32_e32 v14, v9, v10
	v_fmamk_f32 v10, v22, 0x3fb8aa3b, v30
	v_exp_f32_e32 v10, v10
	v_fmamk_f32 v11, v23, 0x3fb8aa3b, v30
	v_exp_f32_e32 v11, v11
	v_fmamk_f32 v12, v24, 0x3fb8aa3b, v30
	v_exp_f32_e32 v12, v12
	v_fmamk_f32 v13, v25, 0x3fb8aa3b, v30
	v_exp_f32_e32 v13, v13
	v_add_f32_e32 v14, v10, v14
	v_add_f32_e32 v14, v11, v14
	v_add_f32_e32 v14, v12, v14
	v_add_f32_e32 v18, v13, v14
	v_fmamk_f32 v14, v26, 0x3fb8aa3b, v30
	v_exp_f32_e32 v14, v14
	v_fmamk_f32 v15, v27, 0x3fb8aa3b, v30
	v_exp_f32_e32 v15, v15
	v_fmamk_f32 v16, v28, 0x3fb8aa3b, v30
	v_exp_f32_e32 v16, v16
	v_fmac_f32_e32 v30, 0x3fb8aa3b, v29
	v_exp_f32_e32 v17, v30
	v_add_f32_e32 v18, v14, v18
	v_add_f32_e32 v18, v15, v18
	v_add_f32_e32 v18, v16, v18
	v_add_f32_e32 v19, v17, v18
	v_mov_b32_e32 v20, v19
	s_nop 1
	v_permlane16_swap_b32_e32 v19, v20
	v_add_f32_e32 v19, v19, v20
	v_or_b32_e32 v18, 0xc0, v199
	v_mov_b32_e32 v20, v19
	s_nop 1
	v_permlane32_swap_b32_e32 v19, v20
	v_cmp_gt_u32_e32 vcc, s4, v18
	s_and_saveexec_b64 s[4:5], vcc
	s_cbranch_execz .LBB0_122
	v_add_f32_e32 v19, v19, v20
	v_rcp_f32_e32 v20, v19
	v_lshl_add_u32 v18, v18, 3, v186
	v_pk_mul_f32 v[2:3], v[20:21], v[2:3] op_sel_hi:[0,1]
	v_pk_mul_f32 v[4:5], v[20:21], v[4:5] op_sel_hi:[0,1]
	v_cvt_pk_f16_f32 v2, v2, v3
	v_cvt_pk_f16_f32 v3, v4, v5
	ds_write_b64 v18, v[2:3]
	v_pk_mul_f32 v[2:3], v[20:21], v[6:7] op_sel_hi:[0,1]
	v_pk_mul_f32 v[4:5], v[20:21], v[8:9] op_sel_hi:[0,1]
	v_cvt_pk_f16_f32 v2, v2, v3
	v_cvt_pk_f16_f32 v3, v4, v5
	ds_write_b64 v18, v[2:3] offset:6464
	v_pk_mul_f32 v[2:3], v[20:21], v[10:11] op_sel_hi:[0,1]
	v_pk_mul_f32 v[4:5], v[20:21], v[12:13] op_sel_hi:[0,1]
	v_cvt_pk_f16_f32 v2, v2, v3
	v_cvt_pk_f16_f32 v3, v4, v5
	ds_write_b64 v18, v[2:3] offset:12928
	v_pk_mul_f32 v[2:3], v[20:21], v[14:15] op_sel_hi:[0,1]
	v_pk_mul_f32 v[4:5], v[20:21], v[16:17] op_sel_hi:[0,1]
	v_cvt_pk_f16_f32 v2, v2, v3
	v_cvt_pk_f16_f32 v3, v4, v5
	ds_write_b64 v18, v[2:3] offset:19392
